# baseline (speedup 1.0000x reference)
_Z6k_gemmIN2pg6EpiLinILi0EEELi768EEvNS0_4GemmET_:
	s_lshr_b32 s3, s2, 3
	s_and_b32 s3, s3, 3
.Lstag7_loop:
	s_cmp_eq_u32 s3, 0
	s_cbranch_scc1 .Lstag7_done
	s_sleep 37
	s_sub_u32 s3, s3, 1
	s_branch .Lstag7_loop
.Lstag7_done:
	s_load_dwordx2 s[4:5], s[0:1], 0x10
	v_readfirstlane_b32 s36, v0
	s_waitcnt lgkmcnt(0)
	s_ashr_i32 s3, s4, 31
	s_ashr_i32 s6, s5, 31
	s_lshr_b32 s3, s3, 24
	s_lshr_b32 s6, s6, 24
	s_add_i32 s3, s4, s3
	s_add_i32 s4, s5, s6
	s_ashr_i32 s3, s3, 8
	s_ashr_i32 s33, s4, 8
	s_mul_i32 s6, s33, s3
	s_cmp_ge_i32 s2, s6
	s_cbranch_scc1 .LBB7_32
	s_ashr_i32 s7, s6, 31
	s_lshr_b32 s4, s7, 29
	s_add_i32 s4, s6, s4
	s_ashr_i32 s37, s4, 3
	s_and_b32 s4, s4, -8
	s_ashr_i32 s39, s2, 31
	s_sub_i32 s38, s6, s4
	s_lshr_b32 s4, s39, 29
	s_add_i32 s10, s2, s4
	s_and_b32 s4, s10, -8
	s_sub_i32 s4, s2, s4
	s_add_i32 s40, s37, 1
	s_cmp_ge_i32 s4, s38
	s_mul_i32 s41, s40, s38
	s_cbranch_scc0 .LBB7_3
	s_sub_i32 s8, s4, s38
	s_mul_i32 s8, s8, s37
	s_add_i32 s11, s8, s41
	s_ashr_i32 s8, s10, 3
	s_cbranch_execz .LBB7_4
	s_branch .LBB7_5

.LBB7_32:
	s_endpgm
	s_endpgm
	s_endpgm
	s_endpgm
	s_endpgm
	s_endpgm
	s_endpgm
	s_endpgm
	s_endpgm
	s_endpgm
	s_endpgm
	s_endpgm
	s_endpgm
	s_endpgm
	s_endpgm
	s_endpgm
	s_endpgm
	s_endpgm
	s_endpgm
	s_endpgm
	s_endpgm
	s_endpgm
	s_endpgm
	s_endpgm
	s_endpgm
	s_endpgm
	s_endpgm
	s_endpgm
	s_endpgm
	s_endpgm
	s_endpgm
	s_endpgm
	s_endpgm
	s_endpgm
	s_endpgm
	s_endpgm
	s_endpgm
	s_endpgm
	s_endpgm
	s_endpgm
	s_endpgm
	s_endpgm
	s_endpgm
	s_endpgm
	s_endpgm
	s_endpgm
	s_endpgm
	s_endpgm
	.section	.rodata,"a",@progbits
	.p2align	6, 0x0

_Z6k_gemmIN2pg6EpiLinILi1EEELi768EEvNS0_4GemmET_:
	s_lshr_b32 s3, s2, 3
	s_and_b32 s3, s3, 3

.LBB9_32:
	s_endpgm
	s_endpgm
	s_endpgm
	s_endpgm
	s_endpgm
	s_endpgm
	s_endpgm
	s_endpgm
	s_endpgm
	s_endpgm
	s_endpgm
	s_endpgm
	s_endpgm
	s_endpgm
	s_endpgm
	s_endpgm
	s_endpgm
	s_endpgm
	s_endpgm
	s_endpgm
	s_endpgm
	s_endpgm
	s_endpgm
	s_endpgm
	s_endpgm
	s_endpgm
	s_endpgm
	s_endpgm
	s_endpgm
	s_endpgm
	s_endpgm
	s_endpgm
	s_endpgm
	s_endpgm
	s_endpgm
	s_endpgm
	s_endpgm
	s_endpgm
	s_endpgm
	s_endpgm
	s_endpgm
	s_endpgm
	s_endpgm
	s_endpgm
	s_endpgm
	s_endpgm
	s_endpgm
	s_endpgm
	s_endpgm
	s_endpgm
	.section	.rodata,"a",@progbits
	.p2align	6, 0x0
